# baseline (speedup 1.0000x reference)
_Z8dog_mainPKfS0_S0_S0_S0_S0_S0_Pf:
	s_load_dwordx8 s[12:19], s[0:1], 0x0
	s_load_dwordx8 s[20:27], s[0:1], 0x20
	s_and_b32 s3, s2, 7
	s_lshl_b32 s3, s3, 5
	s_lshr_b32 s4, s2, 3
	s_add_i32 s4, s3, s4
	s_and_b32 s6, s4, 3
	s_lshr_b32 s7, s4, 2
	s_mov_b32 s5, 0
	s_lshl_b64 s[8:9], s[4:5], 18
	v_and_b32_e32 v1, 63, v0
	v_lshrrev_b32_e32 v2, 6, v0
	v_and_b32_e32 v3, 31, v0
	v_lshl_or_b32 v4, v2, 5, v3
	v_lshlrev_b32_e32 v5, 2, v4
	v_lshlrev_b32_e32 v6, 4, v1
	v_lshl_or_b32 v6, v2, 15, v6
	v_bfe_u32 v7, v0, 5, 1
	s_waitcnt lgkmcnt(0)
	global_load_dword v20, v5, s[18:19]
	global_load_dword v21, v5, s[20:21]
	global_load_dword v22, v5, s[22:23]
	global_load_dword v23, v5, s[24:25]
	global_load_dword v24, v5, s[14:15]
	global_load_dword v25, v5, s[16:17]
	s_add_u32 s12, s12, s8
	s_addc_u32 s13, s13, s9
	v_lshlrev_b32_e32 v6, 4, v1
	v_bfe_u32 v16, v2, 0, 1
	v_lshl_or_b32 v6, v16, 12, v6
	v_bfe_u32 v16, v2, 1, 1
	v_lshl_or_b32 v6, v16, 13, v6
	v_bfe_u32 v16, v2, 2, 1
	v_lshl_or_b32 v6, v16, 14, v6
	global_load_dwordx4 v[128:131], v6, s[12:13] nt
	global_load_dwordx4 v[132:135], v6, s[12:13] offset:1024 nt
	global_load_dwordx4 v[136:139], v6, s[12:13] offset:2048 nt
	global_load_dwordx4 v[140:143], v6, s[12:13] offset:3072 nt
	v_add_u32_e32 v17, 0x8000, v6
	global_load_dwordx4 v[144:147], v17, s[12:13] nt
	v_add_u32_e32 v17, 0x8400, v6
	global_load_dwordx4 v[148:151], v17, s[12:13] nt
	v_add_u32_e32 v17, 0x8800, v6
	global_load_dwordx4 v[152:155], v17, s[12:13] nt
	v_add_u32_e32 v17, 0x8c00, v6
	global_load_dwordx4 v[156:159], v17, s[12:13] nt
	v_add_u32_e32 v17, 0x10000, v6
	global_load_dwordx4 v[160:163], v17, s[12:13] nt
	v_add_u32_e32 v17, 0x10400, v6
	global_load_dwordx4 v[164:167], v17, s[12:13] nt
	v_add_u32_e32 v17, 0x10800, v6
	global_load_dwordx4 v[168:171], v17, s[12:13] nt
	v_add_u32_e32 v17, 0x10c00, v6
	global_load_dwordx4 v[172:175], v17, s[12:13] nt
	v_add_u32_e32 v17, 0x18000, v6
	global_load_dwordx4 v[176:179], v17, s[12:13] nt
	v_add_u32_e32 v17, 0x18400, v6
	global_load_dwordx4 v[180:183], v17, s[12:13] nt
	v_add_u32_e32 v17, 0x18800, v6
	global_load_dwordx4 v[184:187], v17, s[12:13] nt
	v_add_u32_e32 v17, 0x18c00, v6
	global_load_dwordx4 v[188:191], v17, s[12:13] nt
	v_add_u32_e32 v17, 0x20000, v6
	global_load_dwordx4 v[192:195], v17, s[12:13] nt
	v_add_u32_e32 v17, 0x20400, v6
	global_load_dwordx4 v[196:199], v17, s[12:13] nt
	v_add_u32_e32 v17, 0x20800, v6
	global_load_dwordx4 v[200:203], v17, s[12:13] nt
	v_add_u32_e32 v17, 0x20c00, v6
	global_load_dwordx4 v[204:207], v17, s[12:13] nt
	v_add_u32_e32 v17, 0x28000, v6
	global_load_dwordx4 v[208:211], v17, s[12:13] nt
	v_add_u32_e32 v17, 0x28400, v6
	global_load_dwordx4 v[212:215], v17, s[12:13] nt
	v_add_u32_e32 v17, 0x28800, v6
	global_load_dwordx4 v[216:219], v17, s[12:13] nt
	v_add_u32_e32 v17, 0x28c00, v6
	global_load_dwordx4 v[220:223], v17, s[12:13] nt
	v_add_u32_e32 v17, 0x30000, v6
	global_load_dwordx4 v[224:227], v17, s[12:13] nt
	v_add_u32_e32 v17, 0x30400, v6
	global_load_dwordx4 v[228:231], v17, s[12:13] nt
	v_add_u32_e32 v17, 0x30800, v6
	global_load_dwordx4 v[232:235], v17, s[12:13] nt
	v_add_u32_e32 v17, 0x30c00, v6
	global_load_dwordx4 v[236:239], v17, s[12:13] nt
	v_add_u32_e32 v17, 0x38000, v6
	global_load_dwordx4 v[240:243], v17, s[12:13] nt
	v_add_u32_e32 v17, 0x38400, v6
	global_load_dwordx4 v[244:247], v17, s[12:13] nt
	v_add_u32_e32 v17, 0x38800, v6
	global_load_dwordx4 v[248:251], v17, s[12:13] nt
	v_add_u32_e32 v17, 0x38c00, v6
	global_load_dwordx4 v[252:255], v17, s[12:13] nt
	v_and_b32_e32 v16, 1, v0
	v_cmp_eq_u32_e64 s[30:31], 0, v16
	v_and_b32_e32 v17, 2, v0
	v_cmp_eq_u32_e64 s[32:33], 0, v17
	v_lshrrev_b32_e32 v17, 2, v1
	v_lshlrev_b32_e32 v14, 1, v17
	v_bfe_u32 v16, v2, 0, 1
	s_movk_i32 s10, 0x80
	v_mad_u32_u24 v14, v16, s10, v14
	v_bfe_u32 v16, v2, 1, 1
	s_movk_i32 s10, 0x110
	v_mad_u32_u24 v14, v16, s10, v14
	v_bfe_u32 v16, v2, 2, 1
	s_movk_i32 s10, 0x220
	v_mad_u32_u24 v14, v16, s10, v14
	v_bfe_u32 v16, v0, 0, 1
	s_movk_i32 s10, 0x20
	v_mad_u32_u24 v14, v16, s10, v14
	v_bfe_u32 v16, v0, 1, 1
	s_movk_i32 s10, 0x40
	v_mad_u32_u24 v14, v16, s10, v14
	s_movk_i32 s10, 0x110
	v_lshlrev_b32_e32 v17, 4, v7
	v_mad_u32_u24 v15, v3, s10, v17
	s_lshl_b32 s11, s6, 5
	v_lshl_add_u32 v18, v7, 2, s11
	v_cvt_f32_u32_e32 v18, v18
	v_lshlrev_b32_e32 v19, 3, v7
	v_cvt_f32_u32_e32 v19, v19
	s_waitcnt vmcnt(32)
	v_add_f32_e32 v26, v20, v21
	v_rcp_f32_e32 v27, v20
	v_rcp_f32_e32 v28, v26
	v_sub_f32_e32 v12, v19, v22
	v_sub_f32_e32 v13, v18, v23
	v_fma_f32 v29, -v20, v27, 1.0
	v_fma_f32 v30, -v26, v28, 1.0
	v_fma_f32 v27, v29, v27, v27
	v_fma_f32 v28, v30, v28, v28
	v_mul_f32_e32 v8, 0xbf38aa3b, v27
	v_mul_f32_e32 v9, 0xbf38aa3b, v28
	v_mul_f32_e32 v29, v24, v27
	v_mul_f32_e32 v30, v25, v28
	v_mul_f32_e32 v10, 0x3e22f983, v29
	v_mul_f32_e32 v11, 0x3e22f983, v30
	v_mul_f32_e32 v16, v12, v12
	v_add_f32_e32 v17, 0x3f800000, v12
	v_add_f32_e32 v18, 0x40000000, v12
	v_add_f32_e32 v19, 0x40400000, v12
	v_mul_f32_e32 v17, v17, v17
	v_mul_f32_e32 v18, v18, v18
	v_mul_f32_e32 v19, v19, v19
	v_mul_f32_e32 v20, v8, v16
	v_mul_f32_e32 v24, v9, v16
	v_mul_f32_e32 v21, v8, v17
	v_mul_f32_e32 v25, v9, v17
	v_mul_f32_e32 v22, v8, v18
	v_mul_f32_e32 v26, v9, v18
	v_mul_f32_e32 v23, v8, v19
	v_mul_f32_e32 v27, v9, v19
	v_exp_f32_e32 v20, v20
	v_exp_f32_e32 v21, v21
	v_exp_f32_e32 v22, v22
	v_exp_f32_e32 v23, v23
	v_exp_f32_e32 v24, v24
	v_exp_f32_e32 v25, v25
	v_exp_f32_e32 v26, v26
	v_exp_f32_e32 v27, v27
	v_cvt_pk_f16_f32 v32, v20, v21
	v_cvt_pk_f16_f32 v33, v22, v23
	v_cvt_pk_f16_f32 v64, v24, v25
	v_cvt_pk_f16_f32 v65, v26, v27
	v_add_f32_e32 v16, 0x40800000, v12
	v_add_f32_e32 v17, 0x40a00000, v12
	v_add_f32_e32 v18, 0x40c00000, v12
	v_add_f32_e32 v19, 0x40e00000, v12
	v_mul_f32_e32 v16, v16, v16
	v_mul_f32_e32 v17, v17, v17
	v_mul_f32_e32 v18, v18, v18
	v_mul_f32_e32 v19, v19, v19
	v_mul_f32_e32 v20, v8, v16
	v_mul_f32_e32 v24, v9, v16
	v_mul_f32_e32 v21, v8, v17
	v_mul_f32_e32 v25, v9, v17
	v_mul_f32_e32 v22, v8, v18
	v_mul_f32_e32 v26, v9, v18
	v_mul_f32_e32 v23, v8, v19
	v_mul_f32_e32 v27, v9, v19
	v_exp_f32_e32 v20, v20
	v_exp_f32_e32 v21, v21
	v_exp_f32_e32 v22, v22
	v_exp_f32_e32 v23, v23
	v_exp_f32_e32 v24, v24
	v_exp_f32_e32 v25, v25
	v_exp_f32_e32 v26, v26
	v_exp_f32_e32 v27, v27
	v_cvt_pk_f16_f32 v34, v20, v21
	v_cvt_pk_f16_f32 v35, v22, v23
	v_cvt_pk_f16_f32 v66, v24, v25
	v_cvt_pk_f16_f32 v67, v26, v27
	v_add_f32_e32 v16, 0x41800000, v12
	v_add_f32_e32 v17, 0x41880000, v12
	v_add_f32_e32 v18, 0x41900000, v12
	v_add_f32_e32 v19, 0x41980000, v12
	v_mul_f32_e32 v16, v16, v16
	v_mul_f32_e32 v17, v17, v17
	v_mul_f32_e32 v18, v18, v18
	v_mul_f32_e32 v19, v19, v19
	v_mul_f32_e32 v20, v8, v16
	v_mul_f32_e32 v24, v9, v16
	v_mul_f32_e32 v21, v8, v17
	v_mul_f32_e32 v25, v9, v17
	v_mul_f32_e32 v22, v8, v18
	v_mul_f32_e32 v26, v9, v18
	v_mul_f32_e32 v23, v8, v19
	v_mul_f32_e32 v27, v9, v19
	v_exp_f32_e32 v20, v20
	v_exp_f32_e32 v21, v21
	v_exp_f32_e32 v22, v22
	v_exp_f32_e32 v23, v23
	v_exp_f32_e32 v24, v24
	v_exp_f32_e32 v25, v25
	v_exp_f32_e32 v26, v26
	v_exp_f32_e32 v27, v27
	v_cvt_pk_f16_f32 v36, v20, v21
	v_cvt_pk_f16_f32 v37, v22, v23
	v_cvt_pk_f16_f32 v68, v24, v25
	v_cvt_pk_f16_f32 v69, v26, v27
	v_add_f32_e32 v16, 0x41a00000, v12
	v_add_f32_e32 v17, 0x41a80000, v12
	v_add_f32_e32 v18, 0x41b00000, v12
	v_add_f32_e32 v19, 0x41b80000, v12
	v_mul_f32_e32 v16, v16, v16
	v_mul_f32_e32 v17, v17, v17
	v_mul_f32_e32 v18, v18, v18
	v_mul_f32_e32 v19, v19, v19
	v_mul_f32_e32 v20, v8, v16
	v_mul_f32_e32 v24, v9, v16
	v_mul_f32_e32 v21, v8, v17
	v_mul_f32_e32 v25, v9, v17
	v_mul_f32_e32 v22, v8, v18
	v_mul_f32_e32 v26, v9, v18
	v_mul_f32_e32 v23, v8, v19
	v_mul_f32_e32 v27, v9, v19
	v_exp_f32_e32 v20, v20
	v_exp_f32_e32 v21, v21
	v_exp_f32_e32 v22, v22
	v_exp_f32_e32 v23, v23
	v_exp_f32_e32 v24, v24
	v_exp_f32_e32 v25, v25
	v_exp_f32_e32 v26, v26
	v_exp_f32_e32 v27, v27
	v_cvt_pk_f16_f32 v38, v20, v21
	v_cvt_pk_f16_f32 v39, v22, v23
	v_cvt_pk_f16_f32 v70, v24, v25
	v_cvt_pk_f16_f32 v71, v26, v27
	v_add_f32_e32 v16, 0x42000000, v12
	v_add_f32_e32 v17, 0x42040000, v12
	v_add_f32_e32 v18, 0x42080000, v12
	v_add_f32_e32 v19, 0x420c0000, v12
	v_mul_f32_e32 v16, v16, v16
	v_mul_f32_e32 v17, v17, v17
	v_mul_f32_e32 v18, v18, v18
	v_mul_f32_e32 v19, v19, v19
	v_mul_f32_e32 v20, v8, v16
	v_mul_f32_e32 v24, v9, v16
	v_mul_f32_e32 v21, v8, v17
	v_mul_f32_e32 v25, v9, v17
	v_mul_f32_e32 v22, v8, v18
	v_mul_f32_e32 v26, v9, v18
	v_mul_f32_e32 v23, v8, v19
	v_mul_f32_e32 v27, v9, v19
	v_exp_f32_e32 v20, v20
	v_exp_f32_e32 v21, v21
	v_exp_f32_e32 v22, v22
	v_exp_f32_e32 v23, v23
	v_exp_f32_e32 v24, v24
	v_exp_f32_e32 v25, v25
	v_exp_f32_e32 v26, v26
	v_exp_f32_e32 v27, v27
	v_cvt_pk_f16_f32 v40, v20, v21
	v_cvt_pk_f16_f32 v41, v22, v23
	v_cvt_pk_f16_f32 v72, v24, v25
	v_cvt_pk_f16_f32 v73, v26, v27
	v_add_f32_e32 v16, 0x42100000, v12
	v_add_f32_e32 v17, 0x42140000, v12
	v_add_f32_e32 v18, 0x42180000, v12
	v_add_f32_e32 v19, 0x421c0000, v12
	v_mul_f32_e32 v16, v16, v16
	v_mul_f32_e32 v17, v17, v17
	v_mul_f32_e32 v18, v18, v18
	v_mul_f32_e32 v19, v19, v19
	v_mul_f32_e32 v20, v8, v16
	v_mul_f32_e32 v24, v9, v16
	v_mul_f32_e32 v21, v8, v17
	v_mul_f32_e32 v25, v9, v17
	v_mul_f32_e32 v22, v8, v18
	v_mul_f32_e32 v26, v9, v18
	v_mul_f32_e32 v23, v8, v19
	v_mul_f32_e32 v27, v9, v19
	v_exp_f32_e32 v20, v20
	v_exp_f32_e32 v21, v21
	v_exp_f32_e32 v22, v22
	v_exp_f32_e32 v23, v23
	v_exp_f32_e32 v24, v24
	v_exp_f32_e32 v25, v25
	v_exp_f32_e32 v26, v26
	v_exp_f32_e32 v27, v27
	v_cvt_pk_f16_f32 v42, v20, v21
	v_cvt_pk_f16_f32 v43, v22, v23
	v_cvt_pk_f16_f32 v74, v24, v25
	v_cvt_pk_f16_f32 v75, v26, v27
	v_add_f32_e32 v16, 0x42400000, v12
	v_add_f32_e32 v17, 0x42440000, v12
	v_add_f32_e32 v18, 0x42480000, v12
	v_add_f32_e32 v19, 0x424c0000, v12
	v_mul_f32_e32 v16, v16, v16
	v_mul_f32_e32 v17, v17, v17
	v_mul_f32_e32 v18, v18, v18
	v_mul_f32_e32 v19, v19, v19
	v_mul_f32_e32 v20, v8, v16
	v_mul_f32_e32 v24, v9, v16
	v_mul_f32_e32 v21, v8, v17
	v_mul_f32_e32 v25, v9, v17
	v_mul_f32_e32 v22, v8, v18
	v_mul_f32_e32 v26, v9, v18
	v_mul_f32_e32 v23, v8, v19
	v_mul_f32_e32 v27, v9, v19
	v_exp_f32_e32 v20, v20
	v_exp_f32_e32 v21, v21
	v_exp_f32_e32 v22, v22
	v_exp_f32_e32 v23, v23
	v_exp_f32_e32 v24, v24
	v_exp_f32_e32 v25, v25
	v_exp_f32_e32 v26, v26
	v_exp_f32_e32 v27, v27
	v_cvt_pk_f16_f32 v44, v20, v21
	v_cvt_pk_f16_f32 v45, v22, v23
	v_cvt_pk_f16_f32 v76, v24, v25
	v_cvt_pk_f16_f32 v77, v26, v27
	v_add_f32_e32 v16, 0x42500000, v12
	v_add_f32_e32 v17, 0x42540000, v12
	v_add_f32_e32 v18, 0x42580000, v12
	v_add_f32_e32 v19, 0x425c0000, v12
	v_mul_f32_e32 v16, v16, v16
	v_mul_f32_e32 v17, v17, v17
	v_mul_f32_e32 v18, v18, v18
	v_mul_f32_e32 v19, v19, v19
	v_mul_f32_e32 v20, v8, v16
	v_mul_f32_e32 v24, v9, v16
	v_mul_f32_e32 v21, v8, v17
	v_mul_f32_e32 v25, v9, v17
	v_mul_f32_e32 v22, v8, v18
	v_mul_f32_e32 v26, v9, v18
	v_mul_f32_e32 v23, v8, v19
	v_mul_f32_e32 v27, v9, v19
	v_exp_f32_e32 v20, v20
	v_exp_f32_e32 v21, v21
	v_exp_f32_e32 v22, v22
	v_exp_f32_e32 v23, v23
	v_exp_f32_e32 v24, v24
	v_exp_f32_e32 v25, v25
	v_exp_f32_e32 v26, v26
	v_exp_f32_e32 v27, v27
	v_cvt_pk_f16_f32 v46, v20, v21
	v_cvt_pk_f16_f32 v47, v22, v23
	v_cvt_pk_f16_f32 v78, v24, v25
	v_cvt_pk_f16_f32 v79, v26, v27
	v_add_f32_e32 v16, 0x42800000, v12
	v_add_f32_e32 v17, 0x42820000, v12
	v_add_f32_e32 v18, 0x42840000, v12
	v_add_f32_e32 v19, 0x42860000, v12
	v_mul_f32_e32 v16, v16, v16
	v_mul_f32_e32 v17, v17, v17
	v_mul_f32_e32 v18, v18, v18
	v_mul_f32_e32 v19, v19, v19
	v_mul_f32_e32 v20, v8, v16
	v_mul_f32_e32 v24, v9, v16
	v_mul_f32_e32 v21, v8, v17
	v_mul_f32_e32 v25, v9, v17
	v_mul_f32_e32 v22, v8, v18
	v_mul_f32_e32 v26, v9, v18
	v_mul_f32_e32 v23, v8, v19
	v_mul_f32_e32 v27, v9, v19
	v_exp_f32_e32 v20, v20
	v_exp_f32_e32 v21, v21
	v_exp_f32_e32 v22, v22
	v_exp_f32_e32 v23, v23
	v_exp_f32_e32 v24, v24
	v_exp_f32_e32 v25, v25
	v_exp_f32_e32 v26, v26
	v_exp_f32_e32 v27, v27
	v_cvt_pk_f16_f32 v48, v20, v21
	v_cvt_pk_f16_f32 v49, v22, v23
	v_cvt_pk_f16_f32 v80, v24, v25
	v_cvt_pk_f16_f32 v81, v26, v27
	v_add_f32_e32 v16, 0x42880000, v12
	v_add_f32_e32 v17, 0x428a0000, v12
	v_add_f32_e32 v18, 0x428c0000, v12
	v_add_f32_e32 v19, 0x428e0000, v12
	v_mul_f32_e32 v16, v16, v16
	v_mul_f32_e32 v17, v17, v17
	v_mul_f32_e32 v18, v18, v18
	v_mul_f32_e32 v19, v19, v19
	v_mul_f32_e32 v20, v8, v16
	v_mul_f32_e32 v24, v9, v16
	v_mul_f32_e32 v21, v8, v17
	v_mul_f32_e32 v25, v9, v17
	v_mul_f32_e32 v22, v8, v18
	v_mul_f32_e32 v26, v9, v18
	v_mul_f32_e32 v23, v8, v19
	v_mul_f32_e32 v27, v9, v19
	v_exp_f32_e32 v20, v20
	v_exp_f32_e32 v21, v21
	v_exp_f32_e32 v22, v22
	v_exp_f32_e32 v23, v23
	v_exp_f32_e32 v24, v24
	v_exp_f32_e32 v25, v25
	v_exp_f32_e32 v26, v26
	v_exp_f32_e32 v27, v27
	v_cvt_pk_f16_f32 v50, v20, v21
	v_cvt_pk_f16_f32 v51, v22, v23
	v_cvt_pk_f16_f32 v82, v24, v25
	v_cvt_pk_f16_f32 v83, v26, v27
	v_add_f32_e32 v16, 0x42a00000, v12
	v_add_f32_e32 v17, 0x42a20000, v12
	v_add_f32_e32 v18, 0x42a40000, v12
	v_add_f32_e32 v19, 0x42a60000, v12
	v_mul_f32_e32 v16, v16, v16
	v_mul_f32_e32 v17, v17, v17
	v_mul_f32_e32 v18, v18, v18
	v_mul_f32_e32 v19, v19, v19
	v_mul_f32_e32 v20, v8, v16
	v_mul_f32_e32 v24, v9, v16
	v_mul_f32_e32 v21, v8, v17
	v_mul_f32_e32 v25, v9, v17
	v_mul_f32_e32 v22, v8, v18
	v_mul_f32_e32 v26, v9, v18
	v_mul_f32_e32 v23, v8, v19
	v_mul_f32_e32 v27, v9, v19
	v_exp_f32_e32 v20, v20
	v_exp_f32_e32 v21, v21
	v_exp_f32_e32 v22, v22
	v_exp_f32_e32 v23, v23
	v_exp_f32_e32 v24, v24
	v_exp_f32_e32 v25, v25
	v_exp_f32_e32 v26, v26
	v_exp_f32_e32 v27, v27
	v_cvt_pk_f16_f32 v52, v20, v21
	v_cvt_pk_f16_f32 v53, v22, v23
	v_cvt_pk_f16_f32 v84, v24, v25
	v_cvt_pk_f16_f32 v85, v26, v27
	v_add_f32_e32 v16, 0x42a80000, v12
	v_add_f32_e32 v17, 0x42aa0000, v12
	v_add_f32_e32 v18, 0x42ac0000, v12
	v_add_f32_e32 v19, 0x42ae0000, v12
	v_mul_f32_e32 v16, v16, v16
	v_mul_f32_e32 v17, v17, v17
	v_mul_f32_e32 v18, v18, v18
	v_mul_f32_e32 v19, v19, v19
	v_mul_f32_e32 v20, v8, v16
	v_mul_f32_e32 v24, v9, v16
	v_mul_f32_e32 v21, v8, v17
	v_mul_f32_e32 v25, v9, v17
	v_mul_f32_e32 v22, v8, v18
	v_mul_f32_e32 v26, v9, v18
	v_mul_f32_e32 v23, v8, v19
	v_mul_f32_e32 v27, v9, v19
	v_exp_f32_e32 v20, v20
	v_exp_f32_e32 v21, v21
	v_exp_f32_e32 v22, v22
	v_exp_f32_e32 v23, v23
	v_exp_f32_e32 v24, v24
	v_exp_f32_e32 v25, v25
	v_exp_f32_e32 v26, v26
	v_exp_f32_e32 v27, v27
	v_cvt_pk_f16_f32 v54, v20, v21
	v_cvt_pk_f16_f32 v55, v22, v23
	v_cvt_pk_f16_f32 v86, v24, v25
	v_cvt_pk_f16_f32 v87, v26, v27
	v_add_f32_e32 v16, 0x42c00000, v12
	v_add_f32_e32 v17, 0x42c20000, v12
	v_add_f32_e32 v18, 0x42c40000, v12
	v_add_f32_e32 v19, 0x42c60000, v12
	v_mul_f32_e32 v16, v16, v16
	v_mul_f32_e32 v17, v17, v17
	v_mul_f32_e32 v18, v18, v18
	v_mul_f32_e32 v19, v19, v19
	v_mul_f32_e32 v20, v8, v16
	v_mul_f32_e32 v24, v9, v16
	v_mul_f32_e32 v21, v8, v17
	v_mul_f32_e32 v25, v9, v17
	v_mul_f32_e32 v22, v8, v18
	v_mul_f32_e32 v26, v9, v18
	v_mul_f32_e32 v23, v8, v19
	v_mul_f32_e32 v27, v9, v19
	v_exp_f32_e32 v20, v20
	v_exp_f32_e32 v21, v21
	v_exp_f32_e32 v22, v22
	v_exp_f32_e32 v23, v23
	v_exp_f32_e32 v24, v24
	v_exp_f32_e32 v25, v25
	v_exp_f32_e32 v26, v26
	v_exp_f32_e32 v27, v27
	v_cvt_pk_f16_f32 v56, v20, v21
	v_cvt_pk_f16_f32 v57, v22, v23
	v_cvt_pk_f16_f32 v88, v24, v25
	v_cvt_pk_f16_f32 v89, v26, v27
	v_add_f32_e32 v16, 0x42c80000, v12
	v_add_f32_e32 v17, 0x42ca0000, v12
	v_add_f32_e32 v18, 0x42cc0000, v12
	v_add_f32_e32 v19, 0x42ce0000, v12
	v_mul_f32_e32 v16, v16, v16
	v_mul_f32_e32 v17, v17, v17
	v_mul_f32_e32 v18, v18, v18
	v_mul_f32_e32 v19, v19, v19
	v_mul_f32_e32 v20, v8, v16
	v_mul_f32_e32 v24, v9, v16
	v_mul_f32_e32 v21, v8, v17
	v_mul_f32_e32 v25, v9, v17
	v_mul_f32_e32 v22, v8, v18
	v_mul_f32_e32 v26, v9, v18
	v_mul_f32_e32 v23, v8, v19
	v_mul_f32_e32 v27, v9, v19
	v_exp_f32_e32 v20, v20
	v_exp_f32_e32 v21, v21
	v_exp_f32_e32 v22, v22
	v_exp_f32_e32 v23, v23
	v_exp_f32_e32 v24, v24
	v_exp_f32_e32 v25, v25
	v_exp_f32_e32 v26, v26
	v_exp_f32_e32 v27, v27
	v_cvt_pk_f16_f32 v58, v20, v21
	v_cvt_pk_f16_f32 v59, v22, v23
	v_cvt_pk_f16_f32 v90, v24, v25
	v_cvt_pk_f16_f32 v91, v26, v27
	v_add_f32_e32 v16, 0x42e00000, v12
	v_add_f32_e32 v17, 0x42e20000, v12
	v_add_f32_e32 v18, 0x42e40000, v12
	v_add_f32_e32 v19, 0x42e60000, v12
	v_mul_f32_e32 v16, v16, v16
	v_mul_f32_e32 v17, v17, v17
	v_mul_f32_e32 v18, v18, v18
	v_mul_f32_e32 v19, v19, v19
	v_mul_f32_e32 v20, v8, v16
	v_mul_f32_e32 v24, v9, v16
	v_mul_f32_e32 v21, v8, v17
	v_mul_f32_e32 v25, v9, v17
	v_mul_f32_e32 v22, v8, v18
	v_mul_f32_e32 v26, v9, v18
	v_mul_f32_e32 v23, v8, v19
	v_mul_f32_e32 v27, v9, v19
	v_exp_f32_e32 v20, v20
	v_exp_f32_e32 v21, v21
	v_exp_f32_e32 v22, v22
	v_exp_f32_e32 v23, v23
	v_exp_f32_e32 v24, v24
	v_exp_f32_e32 v25, v25
	v_exp_f32_e32 v26, v26
	v_exp_f32_e32 v27, v27
	v_cvt_pk_f16_f32 v60, v20, v21
	v_cvt_pk_f16_f32 v61, v22, v23
	v_cvt_pk_f16_f32 v92, v24, v25
	v_cvt_pk_f16_f32 v93, v26, v27
	v_add_f32_e32 v16, 0x42e80000, v12
	v_add_f32_e32 v17, 0x42ea0000, v12
	v_add_f32_e32 v18, 0x42ec0000, v12
	v_add_f32_e32 v19, 0x42ee0000, v12
	v_mul_f32_e32 v16, v16, v16
	v_mul_f32_e32 v17, v17, v17
	v_mul_f32_e32 v18, v18, v18
	v_mul_f32_e32 v19, v19, v19
	v_mul_f32_e32 v20, v8, v16
	v_mul_f32_e32 v24, v9, v16
	v_mul_f32_e32 v21, v8, v17
	v_mul_f32_e32 v25, v9, v17
	v_mul_f32_e32 v22, v8, v18
	v_mul_f32_e32 v26, v9, v18
	v_mul_f32_e32 v23, v8, v19
	v_mul_f32_e32 v27, v9, v19
	v_exp_f32_e32 v20, v20
	v_exp_f32_e32 v21, v21
	v_exp_f32_e32 v22, v22
	v_exp_f32_e32 v23, v23
	v_exp_f32_e32 v24, v24
	v_exp_f32_e32 v25, v25
	v_exp_f32_e32 v26, v26
	v_exp_f32_e32 v27, v27
	v_cvt_pk_f16_f32 v62, v20, v21
	v_cvt_pk_f16_f32 v63, v22, v23
	v_cvt_pk_f16_f32 v94, v24, v25
	v_cvt_pk_f16_f32 v95, v26, v27
	v_mul_f32_e32 v16, v13, v13
	v_add_f32_e32 v17, 0x3f800000, v13
	v_add_f32_e32 v18, 0x40000000, v13
	v_add_f32_e32 v19, 0x40400000, v13
	v_mul_f32_e32 v17, v17, v17
	v_mul_f32_e32 v18, v18, v18
	v_mul_f32_e32 v19, v19, v19
	v_mul_f32_e32 v20, v8, v16
	v_mul_f32_e32 v24, v9, v16
	v_mul_f32_e32 v21, v8, v17
	v_mul_f32_e32 v25, v9, v17
	v_mul_f32_e32 v22, v8, v18
	v_mul_f32_e32 v26, v9, v18
	v_mul_f32_e32 v23, v8, v19
	v_mul_f32_e32 v27, v9, v19
	v_exp_f32_e32 v20, v20
	v_exp_f32_e32 v21, v21
	v_exp_f32_e32 v22, v22
	v_exp_f32_e32 v23, v23
	v_exp_f32_e32 v24, v24
	v_exp_f32_e32 v25, v25
	v_exp_f32_e32 v26, v26
	v_exp_f32_e32 v27, v27
	v_mul_f32_e32 v96, v10, v20
	v_mul_f32_e32 v97, v10, v21
	v_mul_f32_e32 v98, v10, v22
	v_mul_f32_e32 v99, v10, v23
	v_mul_f32_e32 v112, v11, v24
	v_mul_f32_e32 v113, v11, v25
	v_mul_f32_e32 v114, v11, v26
	v_mul_f32_e32 v115, v11, v27
	v_add_f32_e32 v16, 0x41000000, v13
	v_add_f32_e32 v17, 0x41100000, v13
	v_add_f32_e32 v18, 0x41200000, v13
	v_add_f32_e32 v19, 0x41300000, v13
	v_mul_f32_e32 v16, v16, v16
	v_mul_f32_e32 v17, v17, v17
	v_mul_f32_e32 v18, v18, v18
	v_mul_f32_e32 v19, v19, v19
	v_mul_f32_e32 v20, v8, v16
	v_mul_f32_e32 v24, v9, v16
	v_mul_f32_e32 v21, v8, v17
	v_mul_f32_e32 v25, v9, v17
	v_mul_f32_e32 v22, v8, v18
	v_mul_f32_e32 v26, v9, v18
	v_mul_f32_e32 v23, v8, v19
	v_mul_f32_e32 v27, v9, v19
	v_exp_f32_e32 v20, v20
	v_exp_f32_e32 v21, v21
	v_exp_f32_e32 v22, v22
	v_exp_f32_e32 v23, v23
	v_exp_f32_e32 v24, v24
	v_exp_f32_e32 v25, v25
	v_exp_f32_e32 v26, v26
	v_exp_f32_e32 v27, v27
	v_mul_f32_e32 v100, v10, v20
	v_mul_f32_e32 v101, v10, v21
	v_mul_f32_e32 v102, v10, v22
	v_mul_f32_e32 v103, v10, v23
	v_mul_f32_e32 v116, v11, v24
	v_mul_f32_e32 v117, v11, v25
	v_mul_f32_e32 v118, v11, v26
	v_mul_f32_e32 v119, v11, v27
	v_add_f32_e32 v16, 0x41800000, v13
	v_add_f32_e32 v17, 0x41880000, v13
	v_add_f32_e32 v18, 0x41900000, v13
	v_add_f32_e32 v19, 0x41980000, v13
	v_mul_f32_e32 v16, v16, v16
	v_mul_f32_e32 v17, v17, v17
	v_mul_f32_e32 v18, v18, v18
	v_mul_f32_e32 v19, v19, v19
	v_mul_f32_e32 v20, v8, v16
	v_mul_f32_e32 v24, v9, v16
	v_mul_f32_e32 v21, v8, v17
	v_mul_f32_e32 v25, v9, v17
	v_mul_f32_e32 v22, v8, v18
	v_mul_f32_e32 v26, v9, v18
	v_mul_f32_e32 v23, v8, v19
	v_mul_f32_e32 v27, v9, v19
	v_exp_f32_e32 v20, v20
	v_exp_f32_e32 v21, v21
	v_exp_f32_e32 v22, v22
	v_exp_f32_e32 v23, v23
	v_exp_f32_e32 v24, v24
	v_exp_f32_e32 v25, v25
	v_exp_f32_e32 v26, v26
	v_exp_f32_e32 v27, v27
	v_mul_f32_e32 v104, v10, v20
	v_mul_f32_e32 v105, v10, v21
	v_mul_f32_e32 v106, v10, v22
	v_mul_f32_e32 v107, v10, v23
	v_mul_f32_e32 v120, v11, v24
	v_mul_f32_e32 v121, v11, v25
	v_mul_f32_e32 v122, v11, v26
	v_mul_f32_e32 v123, v11, v27
	v_add_f32_e32 v16, 0x41c00000, v13
	v_add_f32_e32 v17, 0x41c80000, v13
	v_add_f32_e32 v18, 0x41d00000, v13
	v_add_f32_e32 v19, 0x41d80000, v13
	v_mul_f32_e32 v16, v16, v16
	v_mul_f32_e32 v17, v17, v17
	v_mul_f32_e32 v18, v18, v18
	v_mul_f32_e32 v19, v19, v19
	v_mul_f32_e32 v20, v8, v16
	v_mul_f32_e32 v24, v9, v16
	v_mul_f32_e32 v21, v8, v17
	v_mul_f32_e32 v25, v9, v17
	v_mul_f32_e32 v22, v8, v18
	v_mul_f32_e32 v26, v9, v18
	v_mul_f32_e32 v23, v8, v19
	v_mul_f32_e32 v27, v9, v19
	v_exp_f32_e32 v20, v20
	v_exp_f32_e32 v21, v21
	v_exp_f32_e32 v22, v22
	v_exp_f32_e32 v23, v23
	v_exp_f32_e32 v24, v24
	v_exp_f32_e32 v25, v25
	v_exp_f32_e32 v26, v26
	v_exp_f32_e32 v27, v27
	v_mul_f32_e32 v108, v10, v20
	v_mul_f32_e32 v109, v10, v21
	v_mul_f32_e32 v110, v10, v22
	v_mul_f32_e32 v111, v10, v23
	v_mul_f32_e32 v124, v11, v24
	v_mul_f32_e32 v125, v11, v25
	v_mul_f32_e32 v126, v11, v26
	v_mul_f32_e32 v127, v11, v27
	s_waitcnt vmcnt(28)
	v_add_f32_e32 v128, v128, v129
	v_add_f32_e32 v130, v130, v131
	v_add_f32_e32 v132, v132, v133
	v_add_f32_e32 v134, v134, v135
	v_add_f32_e32 v136, v136, v137
	v_add_f32_e32 v138, v138, v139
	v_add_f32_e32 v140, v140, v141
	v_add_f32_e32 v142, v142, v143
	v_add_f32_e32 v128, v128, v130
	v_add_f32_e32 v132, v132, v134
	v_add_f32_e32 v136, v136, v138
	v_add_f32_e32 v140, v140, v142
	v_cndmask_b32_e64 v130, v128, v132, s[30:31]
	v_cndmask_b32_e64 v134, v136, v140, s[30:31]
	v_cndmask_b32_e64 v129, v132, v128, s[30:31]
	v_cndmask_b32_e64 v133, v140, v136, s[30:31]
	v_add_f32_dpp v129, v130, v129 quad_perm:[1,0,3,2] row_mask:0xf bank_mask:0xf bound_ctrl:1
	v_add_f32_dpp v133, v134, v133 quad_perm:[1,0,3,2] row_mask:0xf bank_mask:0xf bound_ctrl:1
	v_cndmask_b32_e64 v135, v129, v133, s[32:33]
	v_cndmask_b32_e64 v131, v133, v129, s[32:33]
	s_nop 1
	v_add_f32_dpp v131, v135, v131 quad_perm:[2,3,0,1] row_mask:0xf bank_mask:0xf bound_ctrl:1
	v_cvt_f16_f32_e32 v131, v131
	ds_write_b16 v14, v131 offset:0
	s_waitcnt vmcnt(24)
	v_add_f32_e32 v144, v144, v145
	v_add_f32_e32 v146, v146, v147
	v_add_f32_e32 v148, v148, v149
	v_add_f32_e32 v150, v150, v151
	v_add_f32_e32 v152, v152, v153
	v_add_f32_e32 v154, v154, v155
	v_add_f32_e32 v156, v156, v157
	v_add_f32_e32 v158, v158, v159
	v_add_f32_e32 v144, v144, v146
	v_add_f32_e32 v148, v148, v150
	v_add_f32_e32 v152, v152, v154
	v_add_f32_e32 v156, v156, v158
	v_cndmask_b32_e64 v146, v144, v148, s[30:31]
	v_cndmask_b32_e64 v150, v152, v156, s[30:31]
	v_cndmask_b32_e64 v145, v148, v144, s[30:31]
	v_cndmask_b32_e64 v149, v156, v152, s[30:31]
	v_add_f32_dpp v145, v146, v145 quad_perm:[1,0,3,2] row_mask:0xf bank_mask:0xf bound_ctrl:1
	v_add_f32_dpp v149, v150, v149 quad_perm:[1,0,3,2] row_mask:0xf bank_mask:0xf bound_ctrl:1
	v_cndmask_b32_e64 v151, v145, v149, s[32:33]
	v_cndmask_b32_e64 v147, v149, v145, s[32:33]
	s_nop 1
	v_add_f32_dpp v147, v151, v147 quad_perm:[2,3,0,1] row_mask:0xf bank_mask:0xf bound_ctrl:1
	v_cvt_f16_f32_e32 v147, v147
	ds_write_b16 v14, v147 offset:1088
	s_waitcnt vmcnt(20)
	v_add_f32_e32 v160, v160, v161
	v_add_f32_e32 v162, v162, v163
	v_add_f32_e32 v164, v164, v165
	v_add_f32_e32 v166, v166, v167
	v_add_f32_e32 v168, v168, v169
	v_add_f32_e32 v170, v170, v171
	v_add_f32_e32 v172, v172, v173
	v_add_f32_e32 v174, v174, v175
	v_add_f32_e32 v160, v160, v162
	v_add_f32_e32 v164, v164, v166
	v_add_f32_e32 v168, v168, v170
	v_add_f32_e32 v172, v172, v174
	v_cndmask_b32_e64 v162, v160, v164, s[30:31]
	v_cndmask_b32_e64 v166, v168, v172, s[30:31]
	v_cndmask_b32_e64 v161, v164, v160, s[30:31]
	v_cndmask_b32_e64 v165, v172, v168, s[30:31]
	v_add_f32_dpp v161, v162, v161 quad_perm:[1,0,3,2] row_mask:0xf bank_mask:0xf bound_ctrl:1
	v_add_f32_dpp v165, v166, v165 quad_perm:[1,0,3,2] row_mask:0xf bank_mask:0xf bound_ctrl:1
	v_cndmask_b32_e64 v167, v161, v165, s[32:33]
	v_cndmask_b32_e64 v163, v165, v161, s[32:33]
	s_nop 1
	v_add_f32_dpp v163, v167, v163 quad_perm:[2,3,0,1] row_mask:0xf bank_mask:0xf bound_ctrl:1
	v_cvt_f16_f32_e32 v163, v163
	ds_write_b16 v14, v163 offset:2176
	s_waitcnt vmcnt(16)
	v_add_f32_e32 v176, v176, v177
	v_add_f32_e32 v178, v178, v179
	v_add_f32_e32 v180, v180, v181
	v_add_f32_e32 v182, v182, v183
	v_add_f32_e32 v184, v184, v185
	v_add_f32_e32 v186, v186, v187
	v_add_f32_e32 v188, v188, v189
	v_add_f32_e32 v190, v190, v191
	v_add_f32_e32 v176, v176, v178
	v_add_f32_e32 v180, v180, v182
	v_add_f32_e32 v184, v184, v186
	v_add_f32_e32 v188, v188, v190
	v_cndmask_b32_e64 v178, v176, v180, s[30:31]
	v_cndmask_b32_e64 v182, v184, v188, s[30:31]
	v_cndmask_b32_e64 v177, v180, v176, s[30:31]
	v_cndmask_b32_e64 v181, v188, v184, s[30:31]
	v_add_f32_dpp v177, v178, v177 quad_perm:[1,0,3,2] row_mask:0xf bank_mask:0xf bound_ctrl:1
	v_add_f32_dpp v181, v182, v181 quad_perm:[1,0,3,2] row_mask:0xf bank_mask:0xf bound_ctrl:1
	v_cndmask_b32_e64 v183, v177, v181, s[32:33]
	v_cndmask_b32_e64 v179, v181, v177, s[32:33]
	s_nop 1
	v_add_f32_dpp v179, v183, v179 quad_perm:[2,3,0,1] row_mask:0xf bank_mask:0xf bound_ctrl:1
	v_cvt_f16_f32_e32 v179, v179
	ds_write_b16 v14, v179 offset:3264
	s_waitcnt vmcnt(12)
	v_add_f32_e32 v192, v192, v193
	v_add_f32_e32 v194, v194, v195
	v_add_f32_e32 v196, v196, v197
	v_add_f32_e32 v198, v198, v199
	v_add_f32_e32 v200, v200, v201
	v_add_f32_e32 v202, v202, v203
	v_add_f32_e32 v204, v204, v205
	v_add_f32_e32 v206, v206, v207
	v_add_f32_e32 v192, v192, v194
	v_add_f32_e32 v196, v196, v198
	v_add_f32_e32 v200, v200, v202
	v_add_f32_e32 v204, v204, v206
	v_cndmask_b32_e64 v194, v192, v196, s[30:31]
	v_cndmask_b32_e64 v198, v200, v204, s[30:31]
	v_cndmask_b32_e64 v193, v196, v192, s[30:31]
	v_cndmask_b32_e64 v197, v204, v200, s[30:31]
	v_add_f32_dpp v193, v194, v193 quad_perm:[1,0,3,2] row_mask:0xf bank_mask:0xf bound_ctrl:1
	v_add_f32_dpp v197, v198, v197 quad_perm:[1,0,3,2] row_mask:0xf bank_mask:0xf bound_ctrl:1
	v_cndmask_b32_e64 v199, v193, v197, s[32:33]
	v_cndmask_b32_e64 v195, v197, v193, s[32:33]
	s_nop 1
	v_add_f32_dpp v195, v199, v195 quad_perm:[2,3,0,1] row_mask:0xf bank_mask:0xf bound_ctrl:1
	v_cvt_f16_f32_e32 v195, v195
	ds_write_b16 v14, v195 offset:4352
	s_waitcnt vmcnt(8)
	v_add_f32_e32 v208, v208, v209
	v_add_f32_e32 v210, v210, v211
	v_add_f32_e32 v212, v212, v213
	v_add_f32_e32 v214, v214, v215
	v_add_f32_e32 v216, v216, v217
	v_add_f32_e32 v218, v218, v219
	v_add_f32_e32 v220, v220, v221
	v_add_f32_e32 v222, v222, v223
	v_add_f32_e32 v208, v208, v210
	v_add_f32_e32 v212, v212, v214
	v_add_f32_e32 v216, v216, v218
	v_add_f32_e32 v220, v220, v222
	v_cndmask_b32_e64 v210, v208, v212, s[30:31]
	v_cndmask_b32_e64 v214, v216, v220, s[30:31]
	v_cndmask_b32_e64 v209, v212, v208, s[30:31]
	v_cndmask_b32_e64 v213, v220, v216, s[30:31]
	v_add_f32_dpp v209, v210, v209 quad_perm:[1,0,3,2] row_mask:0xf bank_mask:0xf bound_ctrl:1
	v_add_f32_dpp v213, v214, v213 quad_perm:[1,0,3,2] row_mask:0xf bank_mask:0xf bound_ctrl:1
	v_cndmask_b32_e64 v215, v209, v213, s[32:33]
	v_cndmask_b32_e64 v211, v213, v209, s[32:33]
	s_nop 1
	v_add_f32_dpp v211, v215, v211 quad_perm:[2,3,0,1] row_mask:0xf bank_mask:0xf bound_ctrl:1
	v_cvt_f16_f32_e32 v211, v211
	ds_write_b16 v14, v211 offset:5440
	s_waitcnt vmcnt(4)
	v_add_f32_e32 v224, v224, v225
	v_add_f32_e32 v226, v226, v227
	v_add_f32_e32 v228, v228, v229
	v_add_f32_e32 v230, v230, v231
	v_add_f32_e32 v232, v232, v233
	v_add_f32_e32 v234, v234, v235
	v_add_f32_e32 v236, v236, v237
	v_add_f32_e32 v238, v238, v239
	v_add_f32_e32 v224, v224, v226
	v_add_f32_e32 v228, v228, v230
	v_add_f32_e32 v232, v232, v234
	v_add_f32_e32 v236, v236, v238
	v_cndmask_b32_e64 v226, v224, v228, s[30:31]
	v_cndmask_b32_e64 v230, v232, v236, s[30:31]
	v_cndmask_b32_e64 v225, v228, v224, s[30:31]
	v_cndmask_b32_e64 v229, v236, v232, s[30:31]
	v_add_f32_dpp v225, v226, v225 quad_perm:[1,0,3,2] row_mask:0xf bank_mask:0xf bound_ctrl:1
	v_add_f32_dpp v229, v230, v229 quad_perm:[1,0,3,2] row_mask:0xf bank_mask:0xf bound_ctrl:1
	v_cndmask_b32_e64 v231, v225, v229, s[32:33]
	v_cndmask_b32_e64 v227, v229, v225, s[32:33]
	s_nop 1
	v_add_f32_dpp v227, v231, v227 quad_perm:[2,3,0,1] row_mask:0xf bank_mask:0xf bound_ctrl:1
	v_cvt_f16_f32_e32 v227, v227
	ds_write_b16 v14, v227 offset:6528
	s_waitcnt vmcnt(0)
	v_add_f32_e32 v240, v240, v241
	v_add_f32_e32 v242, v242, v243
	v_add_f32_e32 v244, v244, v245
	v_add_f32_e32 v246, v246, v247
	v_add_f32_e32 v248, v248, v249
	v_add_f32_e32 v250, v250, v251
	v_add_f32_e32 v252, v252, v253
	v_add_f32_e32 v254, v254, v255
	v_add_f32_e32 v240, v240, v242
	v_add_f32_e32 v244, v244, v246
	v_add_f32_e32 v248, v248, v250
	v_add_f32_e32 v252, v252, v254
	v_cndmask_b32_e64 v242, v240, v244, s[30:31]
	v_cndmask_b32_e64 v246, v248, v252, s[30:31]
	v_cndmask_b32_e64 v241, v244, v240, s[30:31]
	v_cndmask_b32_e64 v245, v252, v248, s[30:31]
	v_add_f32_dpp v241, v242, v241 quad_perm:[1,0,3,2] row_mask:0xf bank_mask:0xf bound_ctrl:1
	v_add_f32_dpp v245, v246, v245 quad_perm:[1,0,3,2] row_mask:0xf bank_mask:0xf bound_ctrl:1
	v_cndmask_b32_e64 v247, v241, v245, s[32:33]
	v_cndmask_b32_e64 v243, v245, v241, s[32:33]
	s_nop 1
	v_add_f32_dpp v243, v247, v243 quad_perm:[2,3,0,1] row_mask:0xf bank_mask:0xf bound_ctrl:1
	v_cvt_f16_f32_e32 v243, v243
	ds_write_b16 v14, v243 offset:7616
	s_waitcnt lgkmcnt(0)
	s_barrier
	ds_read_b128 v[160:163], v15 offset:0
	ds_read_b128 v[164:167], v15 offset:32
	ds_read_b128 v[168:171], v15 offset:64
	ds_read_b128 v[172:175], v15 offset:96
	ds_read_b128 v[176:179], v15 offset:128
	ds_read_b128 v[180:183], v15 offset:160
	ds_read_b128 v[184:187], v15 offset:192
	ds_read_b128 v[188:191], v15 offset:224
	s_waitcnt lgkmcnt(7)
	v_mfma_f32_32x32x16_f16 v[128:143], v[160:163], v[32:35], 0
	v_mfma_f32_32x32x16_f16 v[144:159], v[160:163], v[64:67], 0
	s_waitcnt lgkmcnt(6)
	v_mfma_f32_32x32x16_f16 v[128:143], v[164:167], v[36:39], v[128:143]
	v_mfma_f32_32x32x16_f16 v[144:159], v[164:167], v[68:71], v[144:159]
	s_waitcnt lgkmcnt(5)
	v_mfma_f32_32x32x16_f16 v[128:143], v[168:171], v[40:43], v[128:143]
	v_mfma_f32_32x32x16_f16 v[144:159], v[168:171], v[72:75], v[144:159]
	s_waitcnt lgkmcnt(4)
	v_mfma_f32_32x32x16_f16 v[128:143], v[172:175], v[44:47], v[128:143]
	v_mfma_f32_32x32x16_f16 v[144:159], v[172:175], v[76:79], v[144:159]
	s_waitcnt lgkmcnt(3)
	v_mfma_f32_32x32x16_f16 v[128:143], v[176:179], v[48:51], v[128:143]
	v_mfma_f32_32x32x16_f16 v[144:159], v[176:179], v[80:83], v[144:159]
	s_waitcnt lgkmcnt(2)
	v_mfma_f32_32x32x16_f16 v[128:143], v[180:183], v[52:55], v[128:143]
	v_mfma_f32_32x32x16_f16 v[144:159], v[180:183], v[84:87], v[144:159]
	s_waitcnt lgkmcnt(1)
	v_mfma_f32_32x32x16_f16 v[128:143], v[184:187], v[56:59], v[128:143]
	v_mfma_f32_32x32x16_f16 v[144:159], v[184:187], v[88:91], v[144:159]
	s_waitcnt lgkmcnt(0)
	v_mfma_f32_32x32x16_f16 v[128:143], v[188:191], v[60:63], v[128:143]
	v_mfma_f32_32x32x16_f16 v[144:159], v[188:191], v[92:95], v[144:159]
	s_nop 15
	s_nop 3
	v_mul_f32_e32 v16, v96, v128
	v_mul_f32_e32 v17, v97, v129
	v_mul_f32_e32 v18, v98, v130
	v_mul_f32_e32 v19, v99, v131
	v_fma_f32 v16, -v112, v144, v16
	v_fma_f32 v17, -v113, v145, v17
	v_fma_f32 v18, -v114, v146, v18
	v_fma_f32 v19, -v115, v147, v19
	v_fma_f32 v16, v100, v132, v16
	v_fma_f32 v16, -v116, v148, v16
	v_fma_f32 v17, v101, v133, v17
	v_fma_f32 v17, -v117, v149, v17
	v_fma_f32 v18, v102, v134, v18
	v_fma_f32 v18, -v118, v150, v18
	v_fma_f32 v19, v103, v135, v19
	v_fma_f32 v19, -v119, v151, v19
	v_fma_f32 v16, v104, v136, v16
	v_fma_f32 v16, -v120, v152, v16
	v_fma_f32 v17, v105, v137, v17
	v_fma_f32 v17, -v121, v153, v17
	v_fma_f32 v18, v106, v138, v18
	v_fma_f32 v18, -v122, v154, v18
	v_fma_f32 v19, v107, v139, v19
	v_fma_f32 v19, -v123, v155, v19
	v_fma_f32 v16, v108, v140, v16
	v_fma_f32 v16, -v124, v156, v16
	v_fma_f32 v17, v109, v141, v17
	v_fma_f32 v17, -v125, v157, v17
	v_fma_f32 v18, v110, v142, v18
	v_fma_f32 v18, -v126, v158, v18
	v_fma_f32 v19, v111, v143, v19
	v_fma_f32 v19, -v127, v159, v19
	v_add_f32_e32 v16, v16, v17
	v_add_f32_e32 v18, v18, v19
	v_add_f32_e32 v16, v16, v18
	v_mov_b32_e32 v17, v16
	s_lshl_b32 s6, s6, 6
	s_add_i32 s6, s6, s7
	s_lshl_b32 s6, s6, 10
	v_permlane32_swap_b32_e32 v16, v17
	v_add_u32_e32 v5, s6, v5
	v_cmp_gt_u32_e32 vcc, 32, v1
	v_add_f32_e32 v16, v16, v17
	s_and_saveexec_b64 s[2:3], vcc
	s_cbranch_execz .Ldog_main_done
	global_store_dword v5, v16, s[26:27]
